# v22 + DN phase reuses the expert segment table GU left in LDS (no second counter read + scan)
# speedup vs baseline: 1.0607x; 1.0079x over previous
; #define LAS __attribute__((address_space(3)))
; __device__ __forceinline__ int opaque_tid() { int t = threadIdx.x; asm volatile("" : "+v"(t)); return t; }
; __device__ __forceinline__ void seg_to_lds(const Args& a, LAS unsigned char* lds, int layer) {
;     LAS int* seg = (LAS int*)(lds + SEG_OFF);
;     const int t = opaque_tid();
;     if (t < 16) {
;         unsigned* cnt = (unsigned*)(a.ws + WS_CTL) + CW_CNT + layer * 16 * 64;
;         const int c = (int)__hip_atomic_load(cnt + t * 64, __ATOMIC_RELAXED, __HIP_MEMORY_SCOPE_AGENT);
;         const int pad = (c + 255) & ~255;
;         int incl = pad;
; #pragma unroll
;         for (int o2 = 1; o2 < 16; o2 <<= 1) { const int u2 = __shfl_up(incl, o2); if (t >= o2) incl += u2; }
;         seg[t] = c; seg[16 + t] = incl - pad;
;         if (t == 15) seg[32] = incl;
;     }
;     __syncthreads();
; }
.Ldn_entry:
	v_mov_b32_e32 v1, v0
	s_waitcnt lgkmcnt(0)
	s_barrier
	s_nop 0
	v_cmp_gt_i32_e32 vcc, 0, v1
	s_and_saveexec_b64 s[4:5], vcc
	s_cbranch_execz .LBB0_1159
	v_lshlrev_b32_e32 v2, 6, v1
	v_readlane_b32 s6, v254, 22
	v_ashrrev_i32_e32 v3, 31, v2
	v_readlane_b32 s7, v254, 23
	v_cmp_lt_i32_e32 vcc, v235, v240
	s_nop 0
	v_lshl_add_u64 v[2:3], v[2:3], 2, s[6:7]
	global_load_dword v3, v[2:3], off sc1
	v_cndmask_b32_e32 v2, v235, v199, vcc
	v_lshlrev_b32_e32 v2, 2, v2
	v_cmp_lt_i32_e32 vcc, v233, v240
	s_waitcnt vmcnt(0)
	v_add_u32_e32 v4, 0xff, v3
	v_and_b32_e32 v4, 0xffffff00, v4
	ds_bpermute_b32 v2, v2, v4
	v_cndmask_b32_e32 v5, v233, v199, vcc
	v_cmp_lt_i32_e32 vcc, 0, v1
	v_lshlrev_b32_e32 v5, 2, v5
	s_waitcnt lgkmcnt(0)
	v_cndmask_b32_e32 v2, 0, v2, vcc
	v_add_u32_e32 v2, v4, v2
	ds_bpermute_b32 v5, v5, v2
	v_cmp_lt_i32_e32 vcc, v243, v240
	s_nop 1
	v_cndmask_b32_e32 v6, v243, v199, vcc
	v_cmp_lt_i32_e32 vcc, 1, v1
	v_lshlrev_b32_e32 v6, 2, v6
	s_waitcnt lgkmcnt(0)
	v_cndmask_b32_e32 v5, 0, v5, vcc
	v_add_u32_e32 v2, v2, v5
	ds_bpermute_b32 v5, v6, v2
	v_cmp_lt_i32_e32 vcc, v203, v240
	s_nop 1
	v_cndmask_b32_e32 v6, v203, v199, vcc
	v_cmp_lt_i32_e32 vcc, 3, v1
	v_lshlrev_b32_e32 v6, 2, v6
	s_waitcnt lgkmcnt(0)
	v_cndmask_b32_e32 v5, 0, v5, vcc
	v_add_u32_e32 v2, v2, v5
	ds_bpermute_b32 v5, v6, v2
	v_cmp_lt_i32_e32 vcc, 7, v1
	v_lshl_add_u32 v6, v1, 2, 0
	v_add_u32_e32 v6, 0x21e00, v6
	s_waitcnt lgkmcnt(0)
	v_cndmask_b32_e32 v5, 0, v5, vcc
	v_add_u32_e32 v2, v2, v5
	v_sub_u32_e32 v4, v2, v4
	v_cmp_eq_u32_e32 vcc, 15, v1
	ds_write2_b32 v6, v3, v4 offset1:16
	s_and_b64 exec, exec, vcc
	s_cbranch_execz .LBB0_1159
	v_readlane_b32 s2, v253, 58
	s_nop 1
	v_mov_b32_e32 v1, s2
	ds_write_b32 v1, v2
